# cmp: score-MFMA bias quads and clamped running max kept in registers, refreshed only on rescale and at the pass switch; the per-item setup has no VALU left except the LDS address
# speedup vs baseline: 1.0025x; 1.0006x over previous
; #define GAS __attribute__((address_space(1)))
; __device__ __forceinline__ unsigned pk4_fp8(float a, float b, float c, float d) { unsigned w = 0u; w = __builtin_amdgcn_cvt_pk_fp8_f32(a, b, w, false); w = __builtin_amdgcn_cvt_pk_fp8_f32(c, d, w, true); return w; }
; __device__ __forceinline__ void gs8_init(GS8& g, const bf16* qrow32) {
; #pragma unroll
;     for (int i = 0; i < 4; ++i) { const u32x4 w = *(const GAS u32x4*)(qrow32 + 8 * i);
;         g.q8[2 * i] = (int)pk4_fp8(bf_lo(w.x) * 8.f, bf_hi(w.x) * 8.f, bf_lo(w.y) * 8.f, bf_hi(w.y) * 8.f); g.q8[2 * i + 1] = (int)pk4_fp8(bf_lo(w.z) * 8.f, bf_hi(w.z) * 8.f, bf_lo(w.w) * 8.f, bf_hi(w.w) * 8.f); }
; #pragma unroll
;     for (int dt = 0; dt < 8; ++dt) g.o[dt] = (f32x4){0.f, 0.f, 0.f, 0.f};
;     g.m = -1e30f; g.l = 0.f;
; }
.LBB0_1569:
	s_waitcnt vmcnt(0)
	v_lshlrev_b32_e32 v0, 16, v30
	v_mul_f32_e32 v1, 0x41000000, v0
	v_and_b32_e32 v0, 0xffff0000, v30
	v_mul_f32_e32 v30, 0x41000000, v0
	v_lshlrev_b32_e32 v0, 16, v31
	v_mul_f32_e32 v34, 0x41000000, v0
	v_mov_b32_e32 v0, v127
	v_cvt_pk_fp8_f32 v0, v1, v30
	v_and_b32_e32 v1, 0xffff0000, v31
	v_mul_f32_e32 v1, 0x41000000, v1
	s_lshr_b32 s60, s73, 4
	v_cvt_pk_fp8_f32 v0, v34, v1 op_sel:[0,0,1]
	v_lshlrev_b32_e32 v1, 16, v32
	v_mul_f32_e32 v30, 0x41000000, v1
	v_and_b32_e32 v1, 0xffff0000, v32
	v_mul_f32_e32 v31, 0x41000000, v1
	v_mov_b32_e32 v1, v127
	v_cvt_pk_fp8_f32 v1, v30, v31
	v_lshlrev_b32_e32 v32, 16, v33
	v_and_b32_e32 v31, 0xffff0000, v33
	v_mul_f32_e32 v30, 0x41000000, v32
	v_mul_f32_e32 v31, 0x41000000, v31
	v_cvt_pk_fp8_f32 v1, v30, v31 op_sel:[0,0,1]
	v_lshlrev_b32_e32 v30, 16, v2
	v_and_b32_e32 v2, 0xffff0000, v2
	v_mul_f32_e32 v30, 0x41000000, v30
	v_mul_f32_e32 v31, 0x41000000, v2
	v_mov_b32_e32 v2, v127
	v_cvt_pk_fp8_f32 v2, v30, v31
	v_lshlrev_b32_e32 v32, 16, v3
	v_and_b32_e32 v3, 0xffff0000, v3
	v_mul_f32_e32 v30, 0x41000000, v32
	v_mul_f32_e32 v3, 0x41000000, v3
	v_cvt_pk_fp8_f32 v2, v30, v3 op_sel:[0,0,1]
	v_lshlrev_b32_e32 v3, 16, v4
	v_mul_f32_e32 v30, 0x41000000, v3
	v_and_b32_e32 v3, 0xffff0000, v4
	v_mul_f32_e32 v4, 0x41000000, v3
	v_mov_b32_e32 v3, v127
	v_cvt_pk_fp8_f32 v3, v30, v4
	v_lshlrev_b32_e32 v31, 16, v5
	v_and_b32_e32 v5, 0xffff0000, v5
	v_mul_f32_e32 v4, 0x41000000, v31
	v_mul_f32_e32 v5, 0x41000000, v5
	v_cvt_pk_fp8_f32 v3, v4, v5 op_sel:[0,0,1]
	v_lshlrev_b32_e32 v4, 16, v26
	v_mul_f32_e32 v5, 0x41000000, v4
	v_and_b32_e32 v4, 0xffff0000, v26
	v_mul_f32_e32 v26, 0x41000000, v4
	v_mov_b32_e32 v4, v127
	v_cvt_pk_fp8_f32 v4, v5, v26
	v_lshlrev_b32_e32 v30, 16, v27
	v_and_b32_e32 v26, 0xffff0000, v27
	v_mul_f32_e32 v5, 0x41000000, v30
	v_mul_f32_e32 v26, 0x41000000, v26
	v_cvt_pk_fp8_f32 v4, v5, v26 op_sel:[0,0,1]
	v_lshlrev_b32_e32 v5, 16, v28
	v_mul_f32_e32 v26, 0x41000000, v5
	v_and_b32_e32 v5, 0xffff0000, v28
	v_mul_f32_e32 v27, 0x41000000, v5
	v_mov_b32_e32 v5, v127
	v_cvt_pk_fp8_f32 v5, v26, v27
	v_lshlrev_b32_e32 v28, 16, v29
	v_and_b32_e32 v27, 0xffff0000, v29
	v_mul_f32_e32 v26, 0x41000000, v28
	v_mul_f32_e32 v27, 0x41000000, v27
	v_cvt_pk_fp8_f32 v5, v26, v27 op_sel:[0,0,1]
	v_lshlrev_b32_e32 v26, 16, v6
	v_and_b32_e32 v6, 0xffff0000, v6
	v_mul_f32_e32 v26, 0x41000000, v26
	v_mul_f32_e32 v27, 0x41000000, v6
	v_mov_b32_e32 v6, v127
	v_cvt_pk_fp8_f32 v6, v26, v27
	v_lshlrev_b32_e32 v28, 16, v7
	v_and_b32_e32 v7, 0xffff0000, v7
	v_mul_f32_e32 v26, 0x41000000, v28
	v_mul_f32_e32 v7, 0x41000000, v7
	v_cvt_pk_fp8_f32 v6, v26, v7 op_sel:[0,0,1]
	v_lshlrev_b32_e32 v7, 16, v8
	v_mul_f32_e32 v26, 0x41000000, v7
	v_and_b32_e32 v7, 0xffff0000, v8
	v_mul_f32_e32 v8, 0x41000000, v7
	v_mov_b32_e32 v7, v127
	v_cvt_pk_fp8_f32 v7, v26, v8
	v_lshlrev_b32_e32 v27, 16, v9
	v_and_b32_e32 v9, 0xffff0000, v9
	v_mul_f32_e32 v8, 0x41000000, v27
	v_mul_f32_e32 v9, 0x41000000, v9
	v_cvt_pk_fp8_f32 v7, v8, v9 op_sel:[0,0,1]
	v_lshlrev_b32_e32 v8, 16, v22
	v_mul_f32_e32 v9, 0x41000000, v8
	v_and_b32_e32 v8, 0xffff0000, v22
	v_mul_f32_e32 v22, 0x41000000, v8
	v_mov_b32_e32 v8, v127
	v_cvt_pk_fp8_f32 v8, v9, v22
	v_lshlrev_b32_e32 v26, 16, v23
	v_and_b32_e32 v22, 0xffff0000, v23
	v_mul_f32_e32 v9, 0x41000000, v26
	v_mul_f32_e32 v22, 0x41000000, v22
	v_cvt_pk_fp8_f32 v8, v9, v22 op_sel:[0,0,1]
	v_lshlrev_b32_e32 v9, 16, v24
	v_mul_f32_e32 v22, 0x41000000, v9
	v_and_b32_e32 v9, 0xffff0000, v24
	v_mul_f32_e32 v23, 0x41000000, v9
	v_mov_b32_e32 v9, v127
	v_cvt_pk_fp8_f32 v9, v22, v23
	v_lshlrev_b32_e32 v24, 16, v25
	v_and_b32_e32 v23, 0xffff0000, v25
	v_mul_f32_e32 v22, 0x41000000, v24
	v_mul_f32_e32 v23, 0x41000000, v23
	v_cvt_pk_fp8_f32 v9, v22, v23 op_sel:[0,0,1]
	v_lshlrev_b32_e32 v22, 16, v10
	v_and_b32_e32 v10, 0xffff0000, v10
	v_mul_f32_e32 v22, 0x41000000, v22
	v_mul_f32_e32 v23, 0x41000000, v10
	v_mov_b32_e32 v10, v127
	v_cvt_pk_fp8_f32 v10, v22, v23
	v_lshlrev_b32_e32 v24, 16, v11
	v_and_b32_e32 v11, 0xffff0000, v11
	v_mul_f32_e32 v22, 0x41000000, v24
	v_mul_f32_e32 v11, 0x41000000, v11
; #define GAS __attribute__((address_space(1)))
; #define LAS __attribute__((address_space(3)))
; __device__ __forceinline__ unsigned pk4_fp8(float a, float b, float c, float d) { unsigned w = 0u; w = __builtin_amdgcn_cvt_pk_fp8_f32(a, b, w, false); w = __builtin_amdgcn_cvt_pk_fp8_f32(c, d, w, true); return w; }
; __device__ __forceinline__ void gs8_init(GS8& g, const bf16* qrow32) {
; #pragma unroll
;     for (int i = 0; i < 4; ++i) { const u32x4 w = *(const GAS u32x4*)(qrow32 + 8 * i);
;         g.q8[2 * i] = (int)pk4_fp8(bf_lo(w.x) * 8.f, bf_hi(w.x) * 8.f, bf_lo(w.y) * 8.f, bf_hi(w.y) * 8.f); g.q8[2 * i + 1] = (int)pk4_fp8(bf_lo(w.z) * 8.f, bf_hi(w.z) * 8.f, bf_lo(w.w) * 8.f, bf_hi(w.w) * 8.f); }
; #pragma unroll
;     for (int dt = 0; dt < 8; ++dt) g.o[dt] = (f32x4){0.f, 0.f, 0.f, 0.f};
;     g.m = -1e30f; g.l = 0.f;
; }
; __device__ __forceinline__ void cmp_phase(Frame& F) {
;     ...
;         GS8 g0, g1; gs8_init(g0, Q + qoff + 32 * kq); gs8_init(g1, Q + qoff + 4 * HD + 32 * kq);
;         const int nkt = ((4 * cur + 2) >> 6) + 1, nit = 2 * nkt;
;         const int limA = (tokA - 31) >> 4, limB = (tokA + 4 - 31) >> 4;
;         const char* Kb = KC + (size_t)bh * 1024 * HD; const char* Vb = VC + (size_t)bh * 1024 * HD * 2;
;         if (F.tid < 256) { unsigned long long mv = 0ull; if (cur < 16) mv = (F.tid <= cur) ? ~0ull : 0ull; else mv = (F.tid == 0 || F.tid == cur || F.tid == cur - 1) ? ~0ull : 0ull; Ml[F.tid] = mv; }
;         float i0 = 0.f, i1 = 0.f, carry0 = 0.f, carry1 = 0.f;
;         LAS float* impA = imp + (8 * F.wave + (c >> 2)) * 256; LAS float* impB = impA + 4 * 256;
;         ring8_dma(RL, Kb, Vb, F.lds, F.wave);
	v_cvt_pk_fp8_f32 v10, v22, v11 op_sel:[0,0,1]
	v_lshlrev_b32_e32 v11, 16, v12
	v_mul_f32_e32 v22, 0x41000000, v11
	v_and_b32_e32 v11, 0xffff0000, v12
	v_mul_f32_e32 v12, 0x41000000, v11
	v_mov_b32_e32 v11, v127
	v_cvt_pk_fp8_f32 v11, v22, v12
	v_lshlrev_b32_e32 v23, 16, v13
	v_and_b32_e32 v13, 0xffff0000, v13
	v_mul_f32_e32 v12, 0x41000000, v23
	v_mul_f32_e32 v13, 0x41000000, v13
	v_cvt_pk_fp8_f32 v11, v12, v13 op_sel:[0,0,1]
	v_lshlrev_b32_e32 v12, 16, v18
	v_mul_f32_e32 v13, 0x41000000, v12
	v_and_b32_e32 v12, 0xffff0000, v18
	v_mul_f32_e32 v18, 0x41000000, v12
	v_mov_b32_e32 v12, v127
	v_cvt_pk_fp8_f32 v12, v13, v18
	v_lshlrev_b32_e32 v22, 16, v19
	v_and_b32_e32 v18, 0xffff0000, v19
	v_mul_f32_e32 v13, 0x41000000, v22
	v_mul_f32_e32 v18, 0x41000000, v18
	v_cvt_pk_fp8_f32 v12, v13, v18 op_sel:[0,0,1]
	v_lshlrev_b32_e32 v13, 16, v20
	v_mul_f32_e32 v18, 0x41000000, v13
	v_and_b32_e32 v13, 0xffff0000, v20
	v_mul_f32_e32 v19, 0x41000000, v13
	v_mov_b32_e32 v13, v127
	v_cvt_pk_fp8_f32 v13, v18, v19
	v_lshlrev_b32_e32 v20, 16, v21
	v_and_b32_e32 v19, 0xffff0000, v21
	v_mul_f32_e32 v18, 0x41000000, v20
	v_mul_f32_e32 v19, 0x41000000, v19
	v_cvt_pk_fp8_f32 v13, v18, v19 op_sel:[0,0,1]
	v_lshlrev_b32_e32 v18, 16, v14
	v_and_b32_e32 v14, 0xffff0000, v14
	v_mul_f32_e32 v18, 0x41000000, v18
	v_mul_f32_e32 v19, 0x41000000, v14
	v_mov_b32_e32 v14, v127
	v_cvt_pk_fp8_f32 v14, v18, v19
	v_lshlrev_b32_e32 v20, 16, v15
	v_and_b32_e32 v15, 0xffff0000, v15
	v_mul_f32_e32 v18, 0x41000000, v20
	v_mul_f32_e32 v15, 0x41000000, v15
	v_cvt_pk_fp8_f32 v14, v18, v15 op_sel:[0,0,1]
	v_lshlrev_b32_e32 v15, 16, v16
	v_mul_f32_e32 v18, 0x41000000, v15
	v_and_b32_e32 v15, 0xffff0000, v16
	v_mul_f32_e32 v16, 0x41000000, v15
	v_mov_b32_e32 v15, v127
	v_cvt_pk_fp8_f32 v15, v18, v16
	v_lshlrev_b32_e32 v19, 16, v17
	v_and_b32_e32 v17, 0xffff0000, v17
	v_mul_f32_e32 v16, 0x41000000, v19
	v_mul_f32_e32 v17, 0x41000000, v17
	v_cvt_pk_fp8_f32 v15, v16, v17 op_sel:[0,0,1]
	v_subrev_u32_e32 v16, 31, v126
	v_subrev_u32_e32 v17, 27, v126
	v_ashrrev_i32_e32 v16, 4, v16
	v_ashrrev_i32_e32 v17, 4, v17
	v_mov_b32_e32 v44, v127
	v_mov_b32_e32 v45, v127
	v_mov_b32_e32 v46, v127
	v_mov_b32_e32 v47, v127
	s_add_i32 s61, s60, 1
	s_sub_i32 s22, s36, 31
	s_lshl_b32 s78, s60, 6
	v_sub_u32_e32 v186, v116, v17
	v_add_u32_e32 v187, v119, v17
	v_add_u32_e32 v188, v119, v16
	v_sub_u32_e32 v189, v116, v16
	v_mov_b64_e32 v[40:41], v[44:45]
	v_mov_b64_e32 v[36:37], v[44:45]
	v_mov_b64_e32 v[32:33], v[44:45]
	v_mov_b64_e32 v[28:29], v[44:45]
	v_mov_b64_e32 v[24:25], v[44:45]
	v_mov_b64_e32 v[20:21], v[44:45]
	v_mov_b64_e32 v[16:17], v[44:45]
	v_mov_b64_e32 v[78:79], v[46:47]
	v_mov_b64_e32 v[74:75], v[46:47]
	v_mov_b64_e32 v[70:71], v[46:47]
	v_mov_b64_e32 v[66:67], v[46:47]
	v_mov_b64_e32 v[62:63], v[46:47]
	v_mov_b64_e32 v[58:59], v[46:47]
	v_mov_b64_e32 v[54:55], v[46:47]
	v_mov_b64_e32 v[50:51], v[46:47]
	s_mov_b32 s59, 0
	s_lshl_b32 s74, s61, 1
	s_ashr_i32 s75, s22, 4
	s_sub_i32 s76, 0, s60
	s_add_i32 s78, s78, 64
	v_mov_b32_e32 v142, v127
	v_mov_b32_e32 v113, v127
	v_mov_b32_e32 v139, 0xf149f2ca
	v_mov_b32_e32 v192, 0
	s_mov_b32 s79, 63
	s_mov_b32 s80, 0
	v_mov_b32_e32 v193, 0
	v_mov_b64_e32 v[42:43], v[46:47]
	v_mov_b64_e32 v[38:39], v[46:47]
	v_mov_b64_e32 v[34:35], v[46:47]
	v_mov_b64_e32 v[30:31], v[46:47]
	v_mov_b64_e32 v[26:27], v[46:47]
	v_mov_b64_e32 v[22:23], v[46:47]
	v_mov_b64_e32 v[18:19], v[46:47]
	v_mov_b32_e32 v190, 0
	v_mov_b32_e32 v191, 0
	v_mov_b64_e32 v[76:77], v[44:45]
	v_mov_b64_e32 v[72:73], v[44:45]
	v_mov_b64_e32 v[68:69], v[44:45]
	v_mov_b64_e32 v[64:65], v[44:45]
	v_mov_b64_e32 v[60:61], v[44:45]
	v_mov_b64_e32 v[56:57], v[44:45]
	v_mov_b64_e32 v[52:53], v[44:45]
	v_mov_b64_e32 v[48:49], v[44:45]
	v_mov_b32_e32 v141, 0xf149f2ca
	v_mov_b32_e32 v224, 0
	v_mov_b32_e32 v225, 0
	v_mov_b32_e32 v216, 0x80000000
	v_mov_b32_e32 v217, 0x80000000
	v_mov_b32_e32 v218, 0x80000000
	v_mov_b32_e32 v219, 0x80000000
	v_mov_b32_e32 v220, 0x80000000
	v_mov_b32_e32 v221, 0x80000000
	v_mov_b32_e32 v222, 0x80000000
	v_mov_b32_e32 v223, 0x80000000
	s_branch .LBB0_1572

; #define LAS __attribute__((address_space(3)))
; #define SBAR() __builtin_amdgcn_sched_barrier(0)
; template <class G> __device__ __forceinline__ float gs_inv(const G& g) { float l = xsum32(xsum16(g.l)); return l > 0.f ? 1.f / l : 0.f; }
;     i32x8a kf[4];
; #pragma unroll
;     for (int T_ = 0; T_ < 4; ++T_) { kf[T_].lo = *(const LAS i32x4a*)(kl8 + T_ * 16 * K8ST); kf[T_].hi = *(const LAS i32x4a*)(kl8 + T_ * 16 * K8ST + 16); }
;     asm volatile("s_waitcnt lgkmcnt(0)" ::: "memory"); SBAR();
; #pragma unroll
;     for (int T_ = 0; T_ < 4; ++T_) { s0[T_] = __builtin_amdgcn_mfma_scale_f32_16x16x128_f8f6f4(kf[T_], g0.q8, (f32x4){c0, c0, c0, c0}, 0, 0, 0, 0x7f7f7f7f, 0, 0x7c7c7c7c);
;         s1[T_] = __builtin_amdgcn_mfma_scale_f32_16x16x128_f8f6f4(kf[T_], g1.q8, (f32x4){c1, c1, c1, c1}, 0, 0, 0, 0x7f7f7f7f, 0, 0x7c7c7c7c); }
; }
; __device__ __forceinline__ void cmp_phase(Frame& F) {
;     ...
;             if (i == nkt) { i0 = gs_inv(g0); i1 = gs_inv(g1); }
;             const bool p1 = i < nkt; const float r0 = p1 ? smc_ref(g0) : g0.m - __builtin_amdgcn_logf(i0), r1 = p1 ? smc_ref(g1) : g1.m - __builtin_amdgcn_logf(i1);
;             f32x4 s0[4], s1[4];
;             qk8_tile2(s0, s1, g0, g1, sb + klane, -r0, -r1);
.LBB0_1575:
	s_add_i32 s22, s78, s59
	s_cmp_lg_u32 s22, 0
	s_cbranch_scc1 .LBB0_1577
	v_mov_b32_e32 v80, v191
	v_mov_b32_e32 v81, v191
	s_nop 1
	v_permlane16_swap_b32 v80, v81
	v_mov_b32_e32 v82, v190
	v_add_f32_e32 v81, v80, v81
	v_mov_b32_e32 v80, v190
	s_nop 1
	v_permlane16_swap_b32 v80, v82
	v_mov_b32_e32 v83, v81
	v_add_f32_e32 v80, v80, v82
	v_mov_b32_e32 v82, v80
	s_nop 1
	v_permlane32_swap_b32 v81, v83
	s_nop 1
	v_permlane32_swap_b32 v80, v82
	s_nop 0
	v_pk_add_f32 v[80:81], v[80:81], v[82:83]
	s_nop 0
	v_div_scale_f32 v82, s[22:23], v80, v80, 1.0
	v_rcp_f32_e32 v83, v82
	s_nop 0
	v_fma_f32 v84, -v82, v83, 1.0
	v_fmac_f32_e32 v83, v84, v83
	v_div_scale_f32 v84, vcc, 1.0, v80, 1.0
	v_mul_f32_e32 v85, v84, v83
	v_fma_f32 v86, -v82, v85, v84
	v_fmac_f32_e32 v85, v86, v83
	v_fma_f32 v82, -v82, v85, v84
	v_div_scale_f32 v84, s[22:23], v81, v81, 1.0
	v_rcp_f32_e32 v86, v84
	v_div_fmas_f32 v82, v82, v83, v85
	v_div_fixup_f32 v82, v82, v80, 1.0
	v_fma_f32 v83, -v84, v86, 1.0
	v_fmac_f32_e32 v86, v83, v86
	v_div_scale_f32 v83, vcc, 1.0, v81, 1.0
	v_mul_f32_e32 v85, v83, v86
	v_fma_f32 v87, -v84, v85, v83
	v_fmac_f32_e32 v85, v87, v86
	v_fma_f32 v83, -v84, v85, v83
	v_div_fmas_f32 v83, v83, v86, v85
	v_div_fixup_f32 v83, v83, v81, 1.0
	v_cmp_lt_f32_e32 vcc, 0, v81
	s_nop 1
	v_cndmask_b32_e32 v113, 0, v83, vcc
	v_cmp_lt_f32_e32 vcc, 0, v80
	s_nop 1
	v_cndmask_b32_e32 v142, 0, v82, vcc
	v_log_f32_e32 v216, v113
	v_log_f32_e32 v220, v142
	s_nop 0
	v_sub_f32_e32 v216, v141, v216
	v_sub_f32_e32 v220, v139, v220
	v_xor_b32_e32 v216, 0x80000000, v216
	v_xor_b32_e32 v220, 0x80000000, v220
	v_mov_b32_e32 v217, v216
	v_mov_b32_e32 v218, v216
	v_mov_b32_e32 v219, v216
	v_mov_b32_e32 v221, v220
	v_mov_b32_e32 v222, v220
	v_mov_b32_e32 v223, v220
.LBB0_1577:
	s_bitcmp1_b32 s80, 0
	s_cselect_b32 s22, 0x6c00, 0
	s_add_i32 s37, s22, 0
	v_add3_u32 v88, s37, v174, v118
	ds_read_b128 v[80:83], v88
	ds_read_b128 v[84:87], v88 offset:16
	ds_read_b128 v[92:95], v88 offset:2304
	ds_read_b128 v[96:99], v88 offset:2320
	ds_read_b128 v[144:147], v88 offset:4608
	ds_read_b128 v[148:151], v88 offset:4624
	ds_read_b128 v[152:155], v88 offset:6912
	ds_read_b128 v[156:159], v88 offset:6928
	s_cmp_le_u32 s80, s60
	s_cselect_b64 s[56:57], -1, 0
	s_cmp_gt_u32 s80, s60
	s_cselect_b64 vcc, -1, 0
	s_and_b64 s[22:23], vcc, exec
	s_cselect_b32 s48, s61, 0
	s_waitcnt lgkmcnt(6)
	v_mfma_scale_f32_16x16x128_f8f6f4 v[108:111], v[80:87], v[0:7], v[216:219], v181, v180 op_sel_hi:[0,0,0]
	s_lshl_b32 s22, s48, 6
	s_sub_i32 s48, 0, s22
	s_sub_i32 s23, s79, s22
	s_cmp_le_i32 s23, s75
	v_mfma_scale_f32_16x16x128_f8f6f4 v[88:91], v[80:87], v[8:15], v[220:223], v181, v180 op_sel_hi:[0,0,0]
	s_waitcnt lgkmcnt(4)
	v_mfma_scale_f32_16x16x128_f8f6f4 v[104:107], v[92:99], v[0:7], v[216:219], v181, v180 op_sel_hi:[0,0,0]
	v_mfma_scale_f32_16x16x128_f8f6f4 v[84:87], v[92:99], v[8:15], v[220:223], v181, v180 op_sel_hi:[0,0,0]
	s_waitcnt lgkmcnt(2)
	v_mfma_scale_f32_16x16x128_f8f6f4 v[100:103], v[144:151], v[0:7], v[216:219], v181, v180 op_sel_hi:[0,0,0]
	v_mfma_scale_f32_16x16x128_f8f6f4 v[80:83], v[144:151], v[8:15], v[220:223], v181, v180 op_sel_hi:[0,0,0]
	s_waitcnt lgkmcnt(0)
	v_mfma_scale_f32_16x16x128_f8f6f4 v[96:99], v[152:159], v[0:7], v[216:219], v181, v180 op_sel_hi:[0,0,0]
	v_mfma_scale_f32_16x16x128_f8f6f4 v[92:95], v[152:159], v[8:15], v[220:223], v181, v180 op_sel_hi:[0,0,0]
	s_cbranch_scc1 .LBB0_1579
; __device__ __forceinline__ float xmax16(float v) { float a = v, b = v; PL_SWAP16(a, b); return fmaxf(a, b); }
; __device__ __forceinline__ float xmax32(float v) { float a = v, b = v; PL_SWAP32(a, b); return fmaxf(a, b); }
; __device__ __forceinline__ void mask_scores(f32x4 (&s)[4], int a, unsigned W, int kb, int q4) {
;     const float NEG = -__builtin_inff();
; #pragma unroll
;     for (int T_ = 0; T_ < 4; ++T_)
; #pragma unroll
;         for (int i = 0; i < 4; ++i) if ((unsigned)(a - (kb + 16 * T_ + 4 * q4 + i)) >= W) s[T_][i] = NEG;
; }
; template <bool WITH_O, class G> __device__ __forceinline__ void online_smc(f32x4 (&s)[4], G& g, const float ref) {
;     float mx = s[0][0];
; #pragma unroll
;     for (int T_ = 0; T_ < 4; ++T_)
; #pragma unroll
;         for (int i = 0; i < 4; ++i) mx = fmaxf(mx, s[T_][i]);
;     const float t = mx + ref;
;     if (!__all(t <= g.m + SM_THR)) {
;         const float mr = xmax32(xmax16(t));
;         const float mn = fmaxf(g.m, mr); const float al = __builtin_amdgcn_exp2f(g.m - mn); g.m = mn; g.l *= al;
;         if (WITH_O) {
; #pragma unroll
;             for (int dt = 0; dt < 8; ++dt) g.o[dt] = g.o[dt] * al; }
;         const float d = ref - mn;
; #pragma unroll
;         for (int T_ = 0; T_ < 4; ++T_)
; #pragma unroll
;             for (int i = 0; i < 4; ++i) s[T_][i] += d;
;     }
	s_add_i32 s22, s22, s59
	s_add_i32 s23, s48, s79
	v_add_u32_e32 v134, s22, v188
	v_add_u32_e32 v144, s23, v189
	v_cmp_gt_u32_e32 vcc, 2.0, v134
	v_subrev_u32_e32 v144, 63, v144
	s_nop 0
	v_cndmask_b32_e32 v108, v182, v108, vcc
	v_cmp_lt_u32_e32 vcc, s69, v144
	v_add_u32_e32 v144, -2, v134
	s_nop 0
	v_cndmask_b32_e32 v109, v182, v109, vcc
	v_cmp_gt_u32_e32 vcc, 2.0, v144
	v_add_u32_e32 v144, -3, v134
	s_nop 0
	v_cndmask_b32_e32 v110, v182, v110, vcc
	v_cmp_gt_u32_e32 vcc, 2.0, v144
	v_add_u32_e32 v144, -16, v134
	s_nop 0
	v_cndmask_b32_e32 v111, v182, v111, vcc
	v_cmp_gt_u32_e32 vcc, 2.0, v144
	v_subrev_u32_e32 v144, 17, v134
	s_nop 0
	v_cndmask_b32_e32 v104, v182, v104, vcc
	v_cmp_gt_u32_e32 vcc, 2.0, v144
	v_subrev_u32_e32 v144, 18, v134
	s_nop 0
	v_cndmask_b32_e32 v105, v182, v105, vcc
	v_cmp_gt_u32_e32 vcc, 2.0, v144
	v_subrev_u32_e32 v144, 19, v134
	s_nop 0
	v_cndmask_b32_e32 v106, v182, v106, vcc
	v_cmp_gt_u32_e32 vcc, 2.0, v144
	v_subrev_u32_e32 v144, 32, v134
	s_nop 0
	v_cndmask_b32_e32 v107, v182, v107, vcc
	v_cmp_gt_u32_e32 vcc, 2.0, v144
	v_subrev_u32_e32 v144, 33, v134
	s_nop 0
	v_cndmask_b32_e32 v100, v182, v100, vcc
	v_cmp_gt_u32_e32 vcc, 2.0, v144
	v_subrev_u32_e32 v144, 34, v134
	s_nop 0
	v_cndmask_b32_e32 v101, v182, v101, vcc
	v_cmp_gt_u32_e32 vcc, 2.0, v144
	v_subrev_u32_e32 v144, 35, v134
	s_nop 0
	v_cndmask_b32_e32 v102, v182, v102, vcc
	v_cmp_gt_u32_e32 vcc, 2.0, v144
	v_subrev_u32_e32 v144, 48, v134
	s_nop 0
	v_cndmask_b32_e32 v103, v182, v103, vcc
	v_cmp_gt_u32_e32 vcc, 2.0, v144
	v_subrev_u32_e32 v144, 49, v134
	s_nop 0
	v_cndmask_b32_e32 v96, v182, v96, vcc
	v_cmp_gt_u32_e32 vcc, 2.0, v144
	v_subrev_u32_e32 v144, 50, v134
	v_subrev_u32_e32 v134, 51, v134
	v_cndmask_b32_e32 v97, v182, v97, vcc
	v_cmp_gt_u32_e32 vcc, 2.0, v144
	v_add_u32_e32 v144, s23, v186
	v_subrev_u32_e32 v144, 63, v144
	v_cndmask_b32_e32 v98, v182, v98, vcc
	v_cmp_gt_u32_e32 vcc, 2.0, v134
	v_add_u32_e32 v134, s22, v187
	s_nop 0
	v_cndmask_b32_e32 v99, v182, v99, vcc
	v_cmp_gt_u32_e32 vcc, 2.0, v134
	s_nop 1
	v_cndmask_b32_e32 v88, v182, v88, vcc
	v_cmp_lt_u32_e32 vcc, s69, v144
	v_add_u32_e32 v144, -2, v134
	s_nop 0
	v_cndmask_b32_e32 v89, v182, v89, vcc
	v_cmp_gt_u32_e32 vcc, 2.0, v144
	v_add_u32_e32 v144, -3, v134
	s_nop 0
	v_cndmask_b32_e32 v90, v182, v90, vcc
	v_cmp_gt_u32_e32 vcc, 2.0, v144
	v_add_u32_e32 v144, -16, v134
	s_nop 0
	v_cndmask_b32_e32 v91, v182, v91, vcc
	v_cmp_gt_u32_e32 vcc, 2.0, v144
	v_subrev_u32_e32 v144, 17, v134
	s_nop 0
	v_cndmask_b32_e32 v84, v182, v84, vcc
	v_cmp_gt_u32_e32 vcc, 2.0, v144
	v_subrev_u32_e32 v144, 18, v134
	s_nop 0
	v_cndmask_b32_e32 v85, v182, v85, vcc
	v_cmp_gt_u32_e32 vcc, 2.0, v144
	v_subrev_u32_e32 v144, 19, v134
	s_nop 0
	v_cndmask_b32_e32 v86, v182, v86, vcc
	v_cmp_gt_u32_e32 vcc, 2.0, v144
	v_subrev_u32_e32 v144, 32, v134
	s_nop 0
	v_cndmask_b32_e32 v87, v182, v87, vcc
	v_cmp_gt_u32_e32 vcc, 2.0, v144
	v_subrev_u32_e32 v144, 33, v134
	s_nop 0
	v_cndmask_b32_e32 v80, v182, v80, vcc
	v_cmp_gt_u32_e32 vcc, 2.0, v144
	v_subrev_u32_e32 v144, 34, v134
	s_nop 0
	v_cndmask_b32_e32 v81, v182, v81, vcc
	v_cmp_gt_u32_e32 vcc, 2.0, v144
	v_subrev_u32_e32 v144, 35, v134
	s_nop 0
	v_cndmask_b32_e32 v82, v182, v82, vcc
	v_cmp_gt_u32_e32 vcc, 2.0, v144
	v_subrev_u32_e32 v144, 48, v134
	s_nop 0
	v_cndmask_b32_e32 v83, v182, v83, vcc
	v_cmp_gt_u32_e32 vcc, 2.0, v144
	v_subrev_u32_e32 v144, 49, v134
	s_nop 0
	v_cndmask_b32_e32 v92, v182, v92, vcc
	v_cmp_gt_u32_e32 vcc, 2.0, v144
	v_subrev_u32_e32 v144, 50, v134
	v_subrev_u32_e32 v134, 51, v134
	v_cndmask_b32_e32 v93, v182, v93, vcc
	v_cmp_gt_u32_e32 vcc, 2.0, v144
	s_nop 1
	v_cndmask_b32_e32 v94, v182, v94, vcc
	v_cmp_gt_u32_e32 vcc, 2.0, v134
	s_nop 1
	v_cndmask_b32_e32 v95, v182, v95, vcc
.LBB0_1579:
	s_mov_b64 s[22:23], -1
	s_and_b64 vcc, exec, s[56:57]
	s_cbranch_vccz .LBB0_1585
	v_add_f32_e32 v159, v141, v135
	v_max_f32_e32 v134, v108, v109
	v_max3_f32 v134, v134, v110, v111
	v_max3_f32 v134, v134, v104, v105
	v_max3_f32 v134, v134, v106, v107
	v_max3_f32 v134, v134, v100, v101
	v_max3_f32 v134, v134, v102, v103
	v_max3_f32 v134, v134, v96, v97
	v_max3_f32 v134, v134, v98, v99
	v_add_f32_e32 v158, v224, v134
	v_cmp_le_f32_e32 vcc, v158, v159
	s_cmp_eq_u64 vcc, exec
	s_cbranch_scc1 .LBB0_1582
	v_mov_b32_e32 v134, v158
	s_nop 1
	v_permlane16_swap_b32 v158, v134
	v_max_f32_e32 v134, v134, v134
	v_max_f32_e32 v144, v158, v158
	v_max_f32_e32 v134, v144, v134
	v_mov_b32_e32 v144, v134
	s_nop 1
	v_permlane32_swap_b32 v134, v144
	v_max3_f32 v194, v141, v134, v144
	v_sub_f32_e32 v134, v141, v194
	v_exp_f32_e32 v134, v134
	v_sub_f32_e32 v144, v224, v194
	v_mul_f32_e32 v191, v191, v134
	v_mov_b32_e32 v141, v194
	v_cmp_ngt_f32_e32 vcc, s68, v141
	v_add_f32_e32 v96, v96, v144
	v_add_f32_e32 v97, v97, v144
	v_add_f32_e32 v98, v98, v144
	v_add_f32_e32 v99, v99, v144
	v_add_f32_e32 v100, v100, v144
	v_add_f32_e32 v101, v101, v144
	v_add_f32_e32 v102, v102, v144
	v_add_f32_e32 v103, v103, v144
	v_add_f32_e32 v104, v104, v144
	v_add_f32_e32 v105, v105, v144
	v_add_f32_e32 v106, v106, v144
	v_add_f32_e32 v107, v107, v144
	v_add_f32_e32 v108, v108, v144
	v_add_f32_e32 v109, v109, v144
	v_add_f32_e32 v110, v110, v144
	v_add_f32_e32 v111, v111, v144
	v_cndmask_b32_e32 v224, 0, v141, vcc
	v_xor_b32_e32 v216, 0x80000000, v224
	v_mov_b32_e32 v217, v216
	v_mov_b32_e32 v218, v216
	v_mov_b32_e32 v219, v216
.LBB0_1582:
	v_max_f32_e32 v134, v88, v89
	v_max3_f32 v134, v134, v90, v91
	v_max3_f32 v134, v134, v84, v85
	v_max3_f32 v134, v134, v86, v87
	v_max3_f32 v134, v134, v80, v81
	v_max3_f32 v134, v134, v82, v83
	v_max3_f32 v134, v134, v92, v93
	v_max3_f32 v134, v134, v94, v95
	v_add_f32_e32 v171, v139, v135
	v_add_f32_e32 v170, v225, v134
	v_cmp_le_f32_e32 vcc, v170, v171
	s_cmp_eq_u64 vcc, exec
	s_cbranch_scc1 .LBB0_1584
	v_mov_b32_e32 v134, v170
	s_nop 1
	v_permlane16_swap_b32 v170, v134
	v_max_f32_e32 v134, v134, v134
	v_max_f32_e32 v144, v170, v170
	v_max_f32_e32 v134, v144, v134
	v_mov_b32_e32 v144, v134
	s_nop 1
	v_permlane32_swap_b32 v134, v144
	v_max3_f32 v134, v139, v134, v144
	v_sub_f32_e32 v144, v139, v134
	v_exp_f32_e32 v144, v144
	v_sub_f32_e32 v138, v225, v134
	v_mul_f32_e32 v190, v190, v144
	v_mov_b32_e32 v139, v134
	v_cmp_ngt_f32_e32 vcc, s68, v139
	v_add_f32_e32 v80, v80, v138
	v_add_f32_e32 v81, v81, v138
	v_add_f32_e32 v82, v82, v138
	v_add_f32_e32 v83, v83, v138
	v_add_f32_e32 v84, v84, v138
	v_add_f32_e32 v85, v85, v138
	v_add_f32_e32 v86, v86, v138
	v_add_f32_e32 v87, v87, v138
	v_add_f32_e32 v88, v88, v138
	v_add_f32_e32 v89, v89, v138
	v_add_f32_e32 v90, v90, v138
	v_add_f32_e32 v91, v91, v138
	v_add_f32_e32 v92, v92, v138
	v_add_f32_e32 v93, v93, v138
	v_add_f32_e32 v94, v94, v138
	v_add_f32_e32 v95, v95, v138
	v_cndmask_b32_e32 v225, 0, v139, vcc
	v_xor_b32_e32 v220, 0x80000000, v225
	v_mov_b32_e32 v221, v220
	v_mov_b32_e32 v222, v220
	v_mov_b32_e32 v223, v220
